# v45 stack plus norm3 p-row load moved early and leader relay atomic dropped; placement padded
# baseline (speedup 1.0000x reference)
.LBB0_139:
	global_load_dword v1, v0, s[10:11] sc1
	s_waitcnt vmcnt(0)
	v_cmp_eq_u32_e32 vcc, 0, v1
	s_cbranch_vccnz .LBB0_141
	s_mov_b64 s[18:19], -1
	s_mov_b64 s[22:23], -1
	s_branch .LBB0_135
	s_nop 0
	s_nop 0

; __device__ __forceinline__ unsigned xb_add(unsigned* p, unsigned v) { return __hip_atomic_fetch_add(p, v, __ATOMIC_RELAXED, __HIP_MEMORY_SCOPE_AGENT); }
; __device__ __forceinline__ void xcd_barrier(const XcdBarrier& b) {
;     ...
;             __builtin_amdgcn_fence(__ATOMIC_ACQUIRE, "agent");
;             xb_add(&bar[XB_XGEN(b.x)], 1u);
;             asm volatile("s_waitcnt vmcnt(0)" ::: "memory");
.LBB0_146:
	s_or_b64 exec, exec, s[6:7]
	s_mov_b64 s[6:7], exec
	v_mbcnt_lo_u32_b32 v0, s6, 0
	v_mbcnt_hi_u32_b32 v0, s7, v0
	v_cmp_eq_u32_e32 vcc, 0, v0
	s_waitcnt vmcnt(0)
	buffer_inv sc1
	s_and_saveexec_b64 s[8:9], vcc
	s_cbranch_execz .LBB0_148
	s_bcnt1_i32_b64 s3, s[6:7]
	v_mov_b32_e32 v0, 0x2000
	v_mov_b32_e32 v1, s3
.LBB0_148:
	s_or_b64 exec, exec, s[8:9]
	s_waitcnt vmcnt(0)

.LBB0_282:
	s_cmp_lt_u32 s3, 0x40001
	s_mov_b64 s[18:19], 0
	s_cselect_b64 s[20:21], -1, 0
	s_mov_b64 s[22:23], -1
	s_and_b64 vcc, exec, s[20:21]
	s_cbranch_vccnz .LBB0_279
	s_branch .LBB0_276
	s_nop 0
	s_nop 0
.LBB0_283:
	s_or_b64 exec, exec, s[14:15]
	s_and_b64 s[14:15], s[16:17], exec

; __device__ __forceinline__ unsigned xb_add(unsigned* p, unsigned v) { return __hip_atomic_fetch_add(p, v, __ATOMIC_RELAXED, __HIP_MEMORY_SCOPE_AGENT); }
; __device__ __forceinline__ void xcd_barrier(const XcdBarrier& b) {
;     ...
;             __builtin_amdgcn_fence(__ATOMIC_ACQUIRE, "agent");
;             xb_add(&bar[XB_XGEN(b.x)], 1u);
;             asm volatile("s_waitcnt vmcnt(0)" ::: "memory");
.LBB0_287:
	s_or_b64 exec, exec, s[6:7]
	s_mov_b64 s[6:7], exec
	v_mbcnt_lo_u32_b32 v0, s6, 0
	v_mbcnt_hi_u32_b32 v0, s7, v0
	v_cmp_eq_u32_e32 vcc, 0, v0
	s_waitcnt vmcnt(0)
	buffer_inv sc1
	s_and_saveexec_b64 s[8:9], vcc
	s_cbranch_execz .LBB0_289
	s_bcnt1_i32_b64 s3, s[6:7]
	v_mov_b32_e32 v0, 0x2000
	v_mov_b32_e32 v1, s3
.LBB0_289:
	s_or_b64 exec, exec, s[8:9]
	s_waitcnt vmcnt(0)

.LBB0_1017:
	s_cmp_lt_u32 s3, 0x40001
	s_mov_b64 s[18:19], 0
	s_cselect_b64 s[20:21], -1, 0
	s_mov_b64 s[22:23], -1
	s_and_b64 vcc, exec, s[20:21]
	s_cbranch_vccnz .LBB0_1014
	s_branch .LBB0_1011
	s_nop 0
	s_nop 0
.LBB0_1018:
	s_or_b64 exec, exec, s[14:15]
	s_and_b64 s[14:15], s[16:17], exec

; __device__ __forceinline__ unsigned xb_add(unsigned* p, unsigned v) { return __hip_atomic_fetch_add(p, v, __ATOMIC_RELAXED, __HIP_MEMORY_SCOPE_AGENT); }
; __device__ __forceinline__ void xcd_barrier(const XcdBarrier& b) {
;     ...
;             __builtin_amdgcn_fence(__ATOMIC_ACQUIRE, "agent");
;             xb_add(&bar[XB_XGEN(b.x)], 1u);
;             asm volatile("s_waitcnt vmcnt(0)" ::: "memory");
.LBB0_1022:
	s_or_b64 exec, exec, s[6:7]
	s_mov_b64 s[6:7], exec
	v_mbcnt_lo_u32_b32 v0, s6, 0
	v_mbcnt_hi_u32_b32 v0, s7, v0
	v_cmp_eq_u32_e32 vcc, 0, v0
	s_waitcnt vmcnt(0)
	buffer_inv sc1
	s_and_saveexec_b64 s[8:9], vcc
	s_cbranch_execz .LBB0_1024
	s_bcnt1_i32_b64 s3, s[6:7]
	v_mov_b32_e32 v0, 0x2000
	v_mov_b32_e32 v1, s3
.LBB0_1024:
	s_or_b64 exec, exec, s[8:9]
	s_waitcnt vmcnt(0)

.LBB0_1115:
	s_cmp_lt_u32 s3, 0x40001
	s_mov_b64 s[18:19], 0
	s_cselect_b64 s[20:21], -1, 0
	s_mov_b64 s[22:23], -1
	s_and_b64 vcc, exec, s[20:21]
	s_cbranch_vccnz .LBB0_1112
	s_branch .LBB0_1109
	s_nop 0
	s_nop 0
.LBB0_1116:
	s_or_b64 exec, exec, s[14:15]
	s_and_b64 s[14:15], s[16:17], exec

; __device__ __forceinline__ unsigned xb_add(unsigned* p, unsigned v) { return __hip_atomic_fetch_add(p, v, __ATOMIC_RELAXED, __HIP_MEMORY_SCOPE_AGENT); }
; __device__ __forceinline__ void xcd_barrier(const XcdBarrier& b) {
;     ...
;             __builtin_amdgcn_fence(__ATOMIC_ACQUIRE, "agent");
;             xb_add(&bar[XB_XGEN(b.x)], 1u);
;             asm volatile("s_waitcnt vmcnt(0)" ::: "memory");
.LBB0_1120:
	s_or_b64 exec, exec, s[6:7]
	s_mov_b64 s[6:7], exec
	v_mbcnt_lo_u32_b32 v0, s6, 0
	v_mbcnt_hi_u32_b32 v0, s7, v0
	v_cmp_eq_u32_e32 vcc, 0, v0
	s_waitcnt vmcnt(0)
	buffer_inv sc1
	s_and_saveexec_b64 s[8:9], vcc
	s_cbranch_execz .LBB0_1122
	s_bcnt1_i32_b64 s3, s[6:7]
	v_mov_b32_e32 v0, 0x2000
	v_mov_b32_e32 v1, s3
.LBB0_1122:
	s_or_b64 exec, exec, s[8:9]
	s_waitcnt vmcnt(0)

.LBB0_1217:
	s_cmp_lt_u32 s3, 0x40001
	s_mov_b64 s[18:19], 0
	s_cselect_b64 s[20:21], -1, 0
	s_mov_b64 s[22:23], -1
	s_and_b64 vcc, exec, s[20:21]
	s_cbranch_vccnz .LBB0_1214
	s_branch .LBB0_1211
	s_nop 0
	s_nop 0
.LBB0_1218:
	s_or_b64 exec, exec, s[14:15]
	s_and_b64 s[14:15], s[16:17], exec

; __device__ __forceinline__ unsigned xb_add(unsigned* p, unsigned v) { return __hip_atomic_fetch_add(p, v, __ATOMIC_RELAXED, __HIP_MEMORY_SCOPE_AGENT); }
; __device__ __forceinline__ void xcd_barrier(const XcdBarrier& b) {
;     ...
;             __builtin_amdgcn_fence(__ATOMIC_ACQUIRE, "agent");
;             xb_add(&bar[XB_XGEN(b.x)], 1u);
;             asm volatile("s_waitcnt vmcnt(0)" ::: "memory");
.LBB0_1222:
	s_or_b64 exec, exec, s[6:7]
	s_mov_b64 s[6:7], exec
	v_mbcnt_lo_u32_b32 v0, s6, 0
	v_mbcnt_hi_u32_b32 v0, s7, v0
	v_cmp_eq_u32_e32 vcc, 0, v0
	s_waitcnt vmcnt(0)
	buffer_inv sc1
	s_and_saveexec_b64 s[8:9], vcc
	s_cbranch_execz .LBB0_1224
	s_bcnt1_i32_b64 s3, s[6:7]
	v_mov_b32_e32 v0, 0x2000
	v_mov_b32_e32 v1, s3
.LBB0_1224:
	s_or_b64 exec, exec, s[8:9]
	s_waitcnt vmcnt(0)

.LBB0_1296:
	s_cmp_lt_u32 s3, 0x40001
	s_mov_b64 s[22:23], 0
	s_cselect_b64 s[24:25], -1, 0
	s_mov_b64 s[26:27], -1
	s_and_b64 vcc, exec, s[24:25]
	s_cbranch_vccnz .LBB0_1293
	s_branch .LBB0_1290
	s_nop 0
	s_nop 0

; __device__ __forceinline__ unsigned xb_add(unsigned* p, unsigned v) { return __hip_atomic_fetch_add(p, v, __ATOMIC_RELAXED, __HIP_MEMORY_SCOPE_AGENT); }
; __device__ __forceinline__ void xcd_barrier(const XcdBarrier& b) {
;     ...
;             __builtin_amdgcn_fence(__ATOMIC_ACQUIRE, "agent");
;             xb_add(&bar[XB_XGEN(b.x)], 1u);
;             asm volatile("s_waitcnt vmcnt(0)" ::: "memory");
.LBB0_1301:
	s_or_b64 exec, exec, s[10:11]
	s_mov_b64 s[10:11], exec
	v_mbcnt_lo_u32_b32 v0, s10, 0
	v_mbcnt_hi_u32_b32 v0, s11, v0
	v_cmp_eq_u32_e32 vcc, 0, v0
	s_waitcnt vmcnt(0)
	buffer_inv sc1
	s_and_saveexec_b64 s[12:13], vcc
	s_cbranch_execz .LBB0_1303
	s_bcnt1_i32_b64 s3, s[10:11]
	v_mov_b32_e32 v0, 0x2000
	v_mov_b32_e32 v1, s3
.LBB0_1303:
	s_or_b64 exec, exec, s[12:13]
	s_waitcnt vmcnt(0)

; __device__ __forceinline__ unsigned xb_add(unsigned* p, unsigned v) { return __hip_atomic_fetch_add(p, v, __ATOMIC_RELAXED, __HIP_MEMORY_SCOPE_AGENT); }
; __device__ __forceinline__ void xcd_barrier(const XcdBarrier& b) {
;     ...
;             __builtin_amdgcn_fence(__ATOMIC_ACQUIRE, "agent");
;             xb_add(&bar[XB_XGEN(b.x)], 1u);
;             asm volatile("s_waitcnt vmcnt(0)" ::: "memory");
.LBB0_1359:
	s_or_b64 exec, exec, s[10:11]
	s_mov_b64 s[10:11], exec
	v_mbcnt_lo_u32_b32 v0, s10, 0
	v_mbcnt_hi_u32_b32 v0, s11, v0
	v_cmp_eq_u32_e32 vcc, 0, v0
	s_waitcnt vmcnt(0)
	buffer_inv sc1
	s_and_saveexec_b64 s[12:13], vcc
	s_cbranch_execz .LBB0_1361
	s_bcnt1_i32_b64 s3, s[10:11]
	v_mov_b32_e32 v0, 0x2000
	v_mov_b32_e32 v1, s3
.LBB0_1361:
	s_or_b64 exec, exec, s[12:13]
	s_waitcnt vmcnt(0)

; __device__ __forceinline__ unsigned xb_add(unsigned* p, unsigned v) { return __hip_atomic_fetch_add(p, v, __ATOMIC_RELAXED, __HIP_MEMORY_SCOPE_AGENT); }
; __device__ __forceinline__ void xcd_barrier(const XcdBarrier& b) {
;     ...
;             __builtin_amdgcn_fence(__ATOMIC_ACQUIRE, "agent");
;             xb_add(&bar[XB_XGEN(b.x)], 1u);
;             asm volatile("s_waitcnt vmcnt(0)" ::: "memory");
.LBB0_1430:
	s_or_b64 exec, exec, s[10:11]
	s_mov_b64 s[10:11], exec
	v_mbcnt_lo_u32_b32 v0, s10, 0
	v_mbcnt_hi_u32_b32 v0, s11, v0
	v_cmp_eq_u32_e32 vcc, 0, v0
	s_waitcnt vmcnt(0)
	buffer_inv sc1
	s_and_saveexec_b64 s[12:13], vcc
	s_cbranch_execz .LBB0_1432
	s_bcnt1_i32_b64 s3, s[10:11]
	v_mov_b32_e32 v0, 0x2000
	v_mov_b32_e32 v1, s3
.LBB0_1432:
	s_or_b64 exec, exec, s[12:13]
	s_waitcnt vmcnt(0)

; __device__ __forceinline__ unsigned xb_add(unsigned* p, unsigned v) { return __hip_atomic_fetch_add(p, v, __ATOMIC_RELAXED, __HIP_MEMORY_SCOPE_AGENT); }
; __device__ __forceinline__ void xcd_barrier(const XcdBarrier& b) {
;     ...
;             __builtin_amdgcn_fence(__ATOMIC_ACQUIRE, "agent");
;             xb_add(&bar[XB_XGEN(b.x)], 1u);
;             asm volatile("s_waitcnt vmcnt(0)" ::: "memory");
.LBB0_1529:
	s_or_b64 exec, exec, s[10:11]
	s_mov_b64 s[10:11], exec
	v_mbcnt_lo_u32_b32 v0, s10, 0
	v_mbcnt_hi_u32_b32 v0, s11, v0
	v_cmp_eq_u32_e32 vcc, 0, v0
	s_waitcnt vmcnt(0)
	buffer_inv sc1
	s_and_saveexec_b64 s[12:13], vcc
	s_cbranch_execz .LBB0_1531
	s_bcnt1_i32_b64 s3, s[10:11]
	v_mov_b32_e32 v0, 0x2000
	v_mov_b32_e32 v1, s3
.LBB0_1531:
	s_or_b64 exec, exec, s[12:13]
	s_waitcnt vmcnt(0)

.LBB0_1631:
	s_cmp_lt_u32 s3, 0x40001
	s_mov_b64 s[18:19], 0
	s_cselect_b64 s[20:21], -1, 0
	s_mov_b64 s[22:23], -1
	s_and_b64 vcc, exec, s[20:21]
	s_cbranch_vccnz .LBB0_1628
	s_branch .LBB0_1625
	s_nop 0
	s_nop 0
.LBB0_1632:
	s_or_b64 exec, exec, s[14:15]
	s_and_b64 s[14:15], s[16:17], exec

; __device__ __forceinline__ unsigned xb_add(unsigned* p, unsigned v) { return __hip_atomic_fetch_add(p, v, __ATOMIC_RELAXED, __HIP_MEMORY_SCOPE_AGENT); }
; __device__ __forceinline__ void xcd_barrier(const XcdBarrier& b) {
;     ...
;             __builtin_amdgcn_fence(__ATOMIC_ACQUIRE, "agent");
;             xb_add(&bar[XB_XGEN(b.x)], 1u);
;             asm volatile("s_waitcnt vmcnt(0)" ::: "memory");
.LBB0_1636:
	s_or_b64 exec, exec, s[6:7]
	s_mov_b64 s[6:7], exec
	v_mbcnt_lo_u32_b32 v0, s6, 0
	v_mbcnt_hi_u32_b32 v0, s7, v0
	v_cmp_eq_u32_e32 vcc, 0, v0
	s_waitcnt vmcnt(0)
	buffer_inv sc1
	s_and_saveexec_b64 s[8:9], vcc
	s_cbranch_execz .LBB0_1638
	s_bcnt1_i32_b64 s3, s[6:7]
	v_mov_b32_e32 v0, 0x2000
	v_mov_b32_e32 v1, s3
.LBB0_1638:
	s_or_b64 exec, exec, s[8:9]
	s_waitcnt vmcnt(0)

; __device__ __forceinline__ unsigned xb_add(unsigned* p, unsigned v) { return __hip_atomic_fetch_add(p, v, __ATOMIC_RELAXED, __HIP_MEMORY_SCOPE_AGENT); }
; __device__ __forceinline__ void xcd_barrier(const XcdBarrier& b) {
;     ...
;             __builtin_amdgcn_fence(__ATOMIC_ACQUIRE, "agent");
;             xb_add(&bar[XB_XGEN(b.x)], 1u);
;             asm volatile("s_waitcnt vmcnt(0)" ::: "memory");
.LBB0_1711:
	s_or_b64 exec, exec, s[6:7]
	s_mov_b64 s[6:7], exec
	v_mbcnt_lo_u32_b32 v0, s6, 0
	v_mbcnt_hi_u32_b32 v0, s7, v0
	v_cmp_eq_u32_e32 vcc, 0, v0
	s_waitcnt vmcnt(0)
	buffer_inv sc1
	s_and_saveexec_b64 s[8:9], vcc
	s_cbranch_execz .LBB0_1713
	s_bcnt1_i32_b64 s3, s[6:7]
	v_mov_b32_e32 v0, 0x2000
	v_mov_b32_e32 v1, s3
.LBB0_1713:
	s_or_b64 exec, exec, s[8:9]
	s_waitcnt vmcnt(0)

.LBB0_1847:
	s_cmp_lt_u32 s3, 0x40001
	s_mov_b64 s[18:19], 0
	s_cselect_b64 s[20:21], -1, 0
	s_mov_b64 s[22:23], -1
	s_and_b64 vcc, exec, s[20:21]
	s_cbranch_vccnz .LBB0_1844
	s_branch .LBB0_1841
	s_nop 0
	s_nop 0
.LBB0_1848:
	s_or_b64 exec, exec, s[14:15]
	s_and_b64 s[14:15], s[16:17], exec

; __device__ __forceinline__ unsigned xb_add(unsigned* p, unsigned v) { return __hip_atomic_fetch_add(p, v, __ATOMIC_RELAXED, __HIP_MEMORY_SCOPE_AGENT); }
; __device__ __forceinline__ void xcd_barrier(const XcdBarrier& b) {
;     ...
;             __builtin_amdgcn_fence(__ATOMIC_ACQUIRE, "agent");
;             xb_add(&bar[XB_XGEN(b.x)], 1u);
;             asm volatile("s_waitcnt vmcnt(0)" ::: "memory");
.LBB0_1852:
	s_or_b64 exec, exec, s[6:7]
	s_mov_b64 s[6:7], exec
	v_mbcnt_lo_u32_b32 v0, s6, 0
	v_mbcnt_hi_u32_b32 v0, s7, v0
	v_cmp_eq_u32_e32 vcc, 0, v0
	s_waitcnt vmcnt(0)
	buffer_inv sc1
	s_and_saveexec_b64 s[8:9], vcc
	s_cbranch_execz .LBB0_1854
	s_bcnt1_i32_b64 s3, s[6:7]
	v_mov_b32_e32 v0, 0x2000
	v_mov_b32_e32 v1, s3
.LBB0_1854:
	s_or_b64 exec, exec, s[8:9]
	s_waitcnt vmcnt(0)

.LBB0_2582:
	s_cmp_lt_u32 s3, 0x40001
	s_mov_b64 s[18:19], 0
	s_cselect_b64 s[20:21], -1, 0
	s_mov_b64 s[22:23], -1
	s_and_b64 vcc, exec, s[20:21]
	s_cbranch_vccnz .LBB0_2579
	s_branch .LBB0_2576
	s_nop 0
	s_nop 0
.LBB0_2583:
	s_or_b64 exec, exec, s[14:15]
	s_and_b64 s[14:15], s[16:17], exec

; __device__ __forceinline__ unsigned xb_add(unsigned* p, unsigned v) { return __hip_atomic_fetch_add(p, v, __ATOMIC_RELAXED, __HIP_MEMORY_SCOPE_AGENT); }
; __device__ __forceinline__ void xcd_barrier(const XcdBarrier& b) {
;     ...
;             __builtin_amdgcn_fence(__ATOMIC_ACQUIRE, "agent");
;             xb_add(&bar[XB_XGEN(b.x)], 1u);
;             asm volatile("s_waitcnt vmcnt(0)" ::: "memory");
.LBB0_2587:
	s_or_b64 exec, exec, s[6:7]
	s_mov_b64 s[6:7], exec
	v_mbcnt_lo_u32_b32 v0, s6, 0
	v_mbcnt_hi_u32_b32 v0, s7, v0
	v_cmp_eq_u32_e32 vcc, 0, v0
	s_waitcnt vmcnt(0)
	buffer_inv sc1
	s_and_saveexec_b64 s[8:9], vcc
	s_cbranch_execz .LBB0_2589
	s_bcnt1_i32_b64 s3, s[6:7]
	v_mov_b32_e32 v0, 0x2000
	v_mov_b32_e32 v1, s3
.LBB0_2589:
	s_or_b64 exec, exec, s[8:9]
	s_waitcnt vmcnt(0)

.LBB0_2680:
	s_cmp_lt_u32 s3, 0x40001
	s_mov_b64 s[18:19], 0
	s_cselect_b64 s[20:21], -1, 0
	s_mov_b64 s[22:23], -1
	s_and_b64 vcc, exec, s[20:21]
	s_cbranch_vccnz .LBB0_2677
	s_branch .LBB0_2674
	s_nop 0
	s_nop 0
.LBB0_2681:
	s_or_b64 exec, exec, s[14:15]
	s_and_b64 s[14:15], s[16:17], exec

; __device__ __forceinline__ unsigned xb_add(unsigned* p, unsigned v) { return __hip_atomic_fetch_add(p, v, __ATOMIC_RELAXED, __HIP_MEMORY_SCOPE_AGENT); }
; __device__ __forceinline__ void xcd_barrier(const XcdBarrier& b) {
;     ...
;             __builtin_amdgcn_fence(__ATOMIC_ACQUIRE, "agent");
;             xb_add(&bar[XB_XGEN(b.x)], 1u);
;             asm volatile("s_waitcnt vmcnt(0)" ::: "memory");
.LBB0_2685:
	s_or_b64 exec, exec, s[6:7]
	s_mov_b64 s[6:7], exec
	v_mbcnt_lo_u32_b32 v0, s6, 0
	v_mbcnt_hi_u32_b32 v0, s7, v0
	v_cmp_eq_u32_e32 vcc, 0, v0
	s_waitcnt vmcnt(0)
	buffer_inv sc1
	s_and_saveexec_b64 s[8:9], vcc
	s_cbranch_execz .LBB0_2687
	s_bcnt1_i32_b64 s3, s[6:7]
	v_mov_b32_e32 v0, 0x2000
	v_mov_b32_e32 v1, s3
.LBB0_2687:
	s_or_b64 exec, exec, s[8:9]
	s_waitcnt vmcnt(0)

.LBB0_2782:
	s_cmp_lt_u32 s3, 0x40001
	s_mov_b64 s[18:19], 0
	s_cselect_b64 s[20:21], -1, 0
	s_mov_b64 s[22:23], -1
	s_and_b64 vcc, exec, s[20:21]
	s_cbranch_vccnz .LBB0_2779
	s_branch .LBB0_2776
	s_nop 0
	s_nop 0
.LBB0_2783:
	s_or_b64 exec, exec, s[14:15]
	s_and_b64 s[14:15], s[16:17], exec

; __device__ __forceinline__ unsigned xb_add(unsigned* p, unsigned v) { return __hip_atomic_fetch_add(p, v, __ATOMIC_RELAXED, __HIP_MEMORY_SCOPE_AGENT); }
; __device__ __forceinline__ void xcd_barrier(const XcdBarrier& b) {
;     ...
;             __builtin_amdgcn_fence(__ATOMIC_ACQUIRE, "agent");
;             xb_add(&bar[XB_XGEN(b.x)], 1u);
;             asm volatile("s_waitcnt vmcnt(0)" ::: "memory");
.LBB0_2787:
	s_or_b64 exec, exec, s[6:7]
	s_mov_b64 s[6:7], exec
	v_mbcnt_lo_u32_b32 v0, s6, 0
	v_mbcnt_hi_u32_b32 v0, s7, v0
	v_cmp_eq_u32_e32 vcc, 0, v0
	s_waitcnt vmcnt(0)
	buffer_inv sc1
	s_and_saveexec_b64 s[8:9], vcc
	s_cbranch_execz .LBB0_2789
	s_bcnt1_i32_b64 s3, s[6:7]
	v_mov_b32_e32 v0, 0x2000
	v_mov_b32_e32 v1, s3
.LBB0_2789:
	s_or_b64 exec, exec, s[8:9]
	s_waitcnt vmcnt(0)

.LBB0_2861:
	s_cmp_lt_u32 s3, 0x40001
	s_mov_b64 s[18:19], 0
	s_cselect_b64 s[20:21], -1, 0
	s_mov_b64 s[22:23], -1
	s_and_b64 vcc, exec, s[20:21]
	s_cbranch_vccnz .LBB0_2858
	s_branch .LBB0_2855
	s_nop 0
	s_nop 0
.LBB0_2862:
	s_or_b64 exec, exec, s[14:15]
	s_and_b64 s[14:15], s[16:17], exec

; __device__ __forceinline__ unsigned xb_add(unsigned* p, unsigned v) { return __hip_atomic_fetch_add(p, v, __ATOMIC_RELAXED, __HIP_MEMORY_SCOPE_AGENT); }
; __device__ __forceinline__ void xcd_barrier(const XcdBarrier& b) {
;     ...
;             __builtin_amdgcn_fence(__ATOMIC_ACQUIRE, "agent");
;             xb_add(&bar[XB_XGEN(b.x)], 1u);
;             asm volatile("s_waitcnt vmcnt(0)" ::: "memory");
.LBB0_2866:
	s_or_b64 exec, exec, s[6:7]
	s_mov_b64 s[6:7], exec
	v_mbcnt_lo_u32_b32 v0, s6, 0
	v_mbcnt_hi_u32_b32 v0, s7, v0
	v_cmp_eq_u32_e32 vcc, 0, v0
	s_waitcnt vmcnt(0)
	buffer_inv sc1
	s_and_saveexec_b64 s[8:9], vcc
	s_cbranch_execz .LBB0_2868
	s_bcnt1_i32_b64 s3, s[6:7]
	v_mov_b32_e32 v0, 0x2000
	v_mov_b32_e32 v1, s3
.LBB0_2868:
	s_or_b64 exec, exec, s[8:9]
	s_waitcnt vmcnt(0)

; __device__ __forceinline__ unsigned xb_add(unsigned* p, unsigned v) { return __hip_atomic_fetch_add(p, v, __ATOMIC_RELAXED, __HIP_MEMORY_SCOPE_AGENT); }
; __device__ __forceinline__ void xcd_barrier(const XcdBarrier& b) {
;     ...
;             __builtin_amdgcn_fence(__ATOMIC_ACQUIRE, "agent");
;             xb_add(&bar[XB_XGEN(b.x)], 1u);
;             asm volatile("s_waitcnt vmcnt(0)" ::: "memory");
.LBB0_2940:
	s_or_b64 exec, exec, s[6:7]
	s_mov_b64 s[6:7], exec
	v_mbcnt_lo_u32_b32 v0, s6, 0
	v_mbcnt_hi_u32_b32 v0, s7, v0
	v_cmp_eq_u32_e32 vcc, 0, v0
	s_waitcnt vmcnt(0)
	buffer_inv sc1
	s_and_saveexec_b64 s[8:9], vcc
	s_cbranch_execz .LBB0_2942
	s_bcnt1_i32_b64 s3, s[6:7]
	v_mov_b32_e32 v0, 0x2000
	v_mov_b32_e32 v1, s3
.LBB0_2942:
	s_or_b64 exec, exec, s[8:9]
	s_waitcnt vmcnt(0)

.LBB0_3087:
	s_cmp_lt_u32 s3, 0x40001
	s_mov_b64 s[18:19], 0
	s_cselect_b64 s[20:21], -1, 0
	s_mov_b64 s[22:23], -1
	s_and_b64 vcc, exec, s[20:21]
	s_cbranch_vccnz .LBB0_3084
	s_branch .LBB0_3081
	s_nop 0
	s_nop 0
.LBB0_3088:
	s_mov_b64 s[12:13], -1
	s_mov_b32 s4, 0

; __device__ __forceinline__ unsigned xb_add(unsigned* p, unsigned v) { return __hip_atomic_fetch_add(p, v, __ATOMIC_RELAXED, __HIP_MEMORY_SCOPE_AGENT); }
; __device__ __forceinline__ void xcd_barrier(const XcdBarrier& b) {
;     ...
;             __builtin_amdgcn_fence(__ATOMIC_ACQUIRE, "agent");
;             xb_add(&bar[XB_XGEN(b.x)], 1u);
;             asm volatile("s_waitcnt vmcnt(0)" ::: "memory");
.LBB0_3096:
	s_or_b64 exec, exec, s[6:7]
	s_mov_b64 s[6:7], exec
	v_mbcnt_lo_u32_b32 v0, s6, 0
	v_mbcnt_hi_u32_b32 v0, s7, v0
	v_cmp_eq_u32_e32 vcc, 0, v0
	s_waitcnt vmcnt(0)
	buffer_inv sc1
	s_and_saveexec_b64 s[8:9], vcc
	s_cbranch_execz .LBB0_3098
	s_bcnt1_i32_b64 s3, s[6:7]
	v_mov_b32_e32 v0, 0x2000
	v_mov_b32_e32 v1, s3
.LBB0_3098:
	s_or_b64 exec, exec, s[8:9]
	s_waitcnt vmcnt(0)

.LBB0_3233:
	s_cmp_lt_u32 s3, 0x40001
	s_mov_b64 s[18:19], 0
	s_cselect_b64 s[20:21], -1, 0
	s_mov_b64 s[22:23], -1
	s_and_b64 vcc, exec, s[20:21]
	s_cbranch_vccnz .LBB0_3230
	s_branch .LBB0_3227
	s_nop 0
	s_nop 0
.LBB0_3234:
	s_or_b64 exec, exec, s[14:15]
	s_and_b64 s[14:15], s[16:17], exec

; __device__ __forceinline__ unsigned xb_add(unsigned* p, unsigned v) { return __hip_atomic_fetch_add(p, v, __ATOMIC_RELAXED, __HIP_MEMORY_SCOPE_AGENT); }
; __device__ __forceinline__ void xcd_barrier(const XcdBarrier& b) {
;     ...
;             __builtin_amdgcn_fence(__ATOMIC_ACQUIRE, "agent");
;             xb_add(&bar[XB_XGEN(b.x)], 1u);
;             asm volatile("s_waitcnt vmcnt(0)" ::: "memory");
.LBB0_3238:
	s_or_b64 exec, exec, s[6:7]
	s_mov_b64 s[6:7], exec
	v_mbcnt_lo_u32_b32 v0, s6, 0
	v_mbcnt_hi_u32_b32 v0, s7, v0
	v_cmp_eq_u32_e32 vcc, 0, v0
	s_waitcnt vmcnt(0)
	buffer_inv sc1
	s_and_saveexec_b64 s[8:9], vcc
	s_cbranch_execz .LBB0_3240
	s_bcnt1_i32_b64 s3, s[6:7]
	v_mov_b32_e32 v0, 0x2000
	v_mov_b32_e32 v1, s3
.LBB0_3240:
	s_or_b64 exec, exec, s[8:9]
	s_waitcnt vmcnt(0)

; DI unsigned pk2(float lo, float hi) { const f32x2 v = {lo, hi}; return __builtin_bit_cast(unsigned, __builtin_convertvector(v, bf16x2_t)); }
; template <int MODE, bool SB  > DI void norm_phase(const Params& P, const Frame& F, int L, const void* src_, const float* gain, bool combine) {
;     ...
;     for (int row = r_lo + F.wave; row < r_hi; row += NWAVES) {
;         f32x4 v[8];
; #pragma unroll
;         for (int j = 0; j < 8; ++j) { if constexpr (SB) v[j] = (f32x4){bflo(vb[j].x), bfhi(vb[j].x), bflo(vb[j].y), bfhi(vb[j].y)}; else v[j] = vn[j]; }
;         { const int rnx = (row + NWAVES < r_hi) ? row + NWAVES : row;
; #pragma unroll
;           for (int j = 0; j < 8; ++j) { if constexpr (SB) vb[j] = *(const u32x2*)(srcb + (size_t)rnx * D + 4 * F.lane + 256 * j); else vn[j] = *(const f32x4*)(src + (size_t)rnx * D + 4 * F.lane + 256 * j); } }
;         if (MODE == 3 && combine) {
;             const int* SLOT = (const int*)(ws + WS_SLOT); const float* TOPW = (const float*)(ws + WS_TOPW); const bf16* Y = (const bf16*)(ws + WS_T + T_YPERM);
;             const int s1 = SLOT[row * 2], s2 = SLOT[row * 2 + 1]; const float w1 = TOPW[row * 2], w2 = TOPW[row * 2 + 1];
;             u32x2 ya[8], yb[8];
; #pragma unroll
;             for (int j = 0; j < 8; ++j) { ya[j] = *(const u32x2*)(Y + (size_t)s1 * D + 4 * F.lane + 256 * j); yb[j] = *(const u32x2*)(Y + (size_t)s2 * D + 4 * F.lane + 256 * j); }
; #pragma unroll
;             for (int j = 0; j < 8; ++j) { const f32x4 y1 = (f32x4){bflo(ya[j].x), bfhi(ya[j].x), bflo(ya[j].y), bfhi(ya[j].y)}, y2 = (f32x4){bflo(yb[j].x), bfhi(yb[j].x), bflo(yb[j].y), bfhi(yb[j].y)};
;                 v[j] = v[j] + w1 * y1 + w2 * y2;
;                 const u32x2 hb = {pk2(v[j][0], v[j][1]), pk2(v[j][2], v[j][3])}; *(u32x2*)(const_cast<bf16*>(srcb) + (size_t)row * D + 4 * F.lane + 256 * j) = hb;
;                 v[j] = (f32x4){bflo(hb.x), bfhi(hb.x), bflo(hb.y), bfhi(hb.y)}; }
;     ...
;         if (MODE == 3) { const f32x4 pv = *(const f32x4*)(P.in[I_P] + ((size_t)L * M + row) * PLE + 4 * F.lane);
;             *((unsigned long long*)((bf16*)(ws + WS_T + T_PB) + (size_t)row * PLE) + F.lane) = (unsigned long long)pk2(pv[0], pv[1]) | ((unsigned long long)pk2(pv[2], pv[3]) << 32); }
.LBB0_3245:
	s_add_i32 s23, s4, 8
	s_cmp_lt_i32 s23, s3
	s_cselect_b64 s[14:15], -1, 0
	s_and_b64 s[24:25], s[14:15], exec
	s_cselect_b32 s4, s23, s4
	s_waitcnt vmcnt(7)
	v_lshlrev_b32_e32 v72, 16, v76
	v_and_b32_e32 v73, 0xffff0000, v76
	v_lshlrev_b32_e32 v74, 16, v77
	v_and_b32_e32 v75, 0xffff0000, v77
	v_lshl_add_u64 v[76:77], s[54:55], 0, v[42:43]
	s_ashr_i32 s7, s6, 31
	s_ashr_i32 s5, s4, 31
	v_add_co_u32_e32 v98, vcc, s20, v76
	s_lshl_b64 s[24:25], s[6:7], 2
	s_lshl_b64 s[4:5], s[4:5], 12
	s_waitcnt vmcnt(6)
	v_lshlrev_b32_e32 v68, 16, v78
	v_and_b32_e32 v69, 0xffff0000, v78
	v_lshlrev_b32_e32 v70, 16, v79
	v_and_b32_e32 v71, 0xffff0000, v79
	v_lshl_add_u64 v[78:79], s[54:55], 0, v[40:41]
	v_addc_co_u32_e32 v99, vcc, 0, v77, vcc
	v_lshl_add_u64 v[100:101], v[32:33], 0, s[4:5]
	s_add_u32 s4, s16, s24
	v_add_co_u32_e32 v92, vcc, s22, v78
	s_addc_u32 s5, s17, s25
	s_waitcnt vmcnt(0)
	v_lshlrev_b32_e32 v44, 16, v90
	v_and_b32_e32 v45, 0xffff0000, v90
	v_lshlrev_b32_e32 v46, 16, v91
	v_and_b32_e32 v47, 0xffff0000, v91
	v_lshlrev_b32_e32 v48, 16, v88
	v_and_b32_e32 v49, 0xffff0000, v88
	v_lshlrev_b32_e32 v50, 16, v89
	v_and_b32_e32 v51, 0xffff0000, v89
	v_lshlrev_b32_e32 v52, 16, v86
	v_and_b32_e32 v53, 0xffff0000, v86
	v_lshlrev_b32_e32 v54, 16, v87
	v_and_b32_e32 v55, 0xffff0000, v87
	v_lshlrev_b32_e32 v56, 16, v84
	v_and_b32_e32 v57, 0xffff0000, v84
	v_lshlrev_b32_e32 v58, 16, v85
	v_and_b32_e32 v59, 0xffff0000, v85
	v_lshlrev_b32_e32 v60, 16, v82
	v_and_b32_e32 v61, 0xffff0000, v82
	v_lshlrev_b32_e32 v62, 16, v83
	v_and_b32_e32 v63, 0xffff0000, v83
	v_lshlrev_b32_e32 v64, 16, v80
	v_and_b32_e32 v65, 0xffff0000, v80
	v_lshlrev_b32_e32 v66, 16, v81
	v_and_b32_e32 v67, 0xffff0000, v81
	v_addc_co_u32_e32 v93, vcc, 0, v79, vcc
	global_load_dwordx2 v[90:91], v[100:101], off
	global_load_dwordx2 v[88:89], v[100:101], off offset:512
	global_load_dwordx2 v[86:87], v[100:101], off offset:1024
	global_load_dwordx2 v[84:85], v[100:101], off offset:1536
	global_load_dwordx2 v[82:83], v[100:101], off offset:2048
	global_load_dwordx2 v[80:81], v[100:101], off offset:2560
	global_load_dwordx2 v[78:79], v[100:101], off offset:3072
	global_load_dwordx2 v[76:77], v[100:101], off offset:3584
	s_add_i32 s26, s6, 1
	global_load_dwordx2 v[100:101], v95, s[4:5]
	s_ashr_i32 s27, s26, 31
	s_add_u32 s4, s18, s24
	s_addc_u32 s5, s19, s25
	s_lshl_b64 s[24:25], s[26:27], 2
	global_load_dword v102, v95, s[4:5]
	s_add_u32 s4, s18, s24
	s_addc_u32 s5, s19, s25
	global_load_dword v104, v95, s[4:5]
	v_mov_b32_e32 v168, 0
	v_mov_b32_e32 v169, 0
	v_mov_b32_e32 v170, 0
	v_mov_b32_e32 v171, 0
	v_mov_b32_e32 v172, 0
	v_mov_b32_e32 v173, 0
	v_mov_b32_e32 v174, 0
	v_mov_b32_e32 v175, 0
	v_lshl_add_u64 v[40:41], v[40:41], 0, s[10:11]
	v_lshl_add_u64 v[42:43], v[42:43], 0, s[12:13]
	s_add_i32 s6, s6, 16
	s_waitcnt vmcnt(2)
	v_ashrrev_i32_e32 v107, 31, v100
	v_mov_b32_e32 v106, v100
	v_ashrrev_i32_e32 v109, 31, v101
	v_mov_b32_e32 v108, v101
	v_lshlrev_b64 v[100:101], 12, v[106:107]
	v_lshlrev_b64 v[106:107], 12, v[108:109]
	v_lshl_add_u64 v[100:101], v[34:35], 0, v[100:101]
	v_lshl_add_u64 v[106:107], v[34:35], 0, v[106:107]
	global_load_dwordx2 v[108:109], v[100:101], off
	global_load_dwordx2 v[110:111], v[106:107], off
	global_load_dwordx2 v[112:113], v[100:101], off offset:512
	global_load_dwordx2 v[114:115], v[106:107], off offset:512
	global_load_dwordx2 v[116:117], v[100:101], off offset:1024
	global_load_dwordx2 v[118:119], v[106:107], off offset:1024
	global_load_dwordx2 v[120:121], v[100:101], off offset:1536
	global_load_dwordx2 v[122:123], v[106:107], off offset:1536
	global_load_dwordx2 v[124:125], v[100:101], off offset:2048
	global_load_dwordx2 v[126:127], v[106:107], off offset:2048
	global_load_dwordx2 v[128:129], v[100:101], off offset:2560
	global_load_dwordx2 v[130:131], v[106:107], off offset:2560
	global_load_dwordx2 v[132:133], v[100:101], off offset:3072
	global_load_dwordx2 v[134:135], v[106:107], off offset:3072
	s_nop 0
	global_load_dwordx2 v[100:101], v[100:101], off offset:3584
	s_nop 0
	global_load_dwordx2 v[106:107], v[106:107], off offset:3584
	global_load_dwordx4 v[176:179], v[38:39], off
	s_waitcnt vmcnt(16)
	v_lshlrev_b32_e32 v136, 16, v108
	v_and_b32_e32 v137, 0xffff0000, v108
	v_lshlrev_b32_e32 v108, 16, v109
	v_and_b32_e32 v109, 0xffff0000, v109
	s_waitcnt vmcnt(14)
	v_lshlrev_b32_e32 v140, 16, v112
	v_and_b32_e32 v141, 0xffff0000, v112
	v_lshlrev_b32_e32 v112, 16, v113
	v_and_b32_e32 v113, 0xffff0000, v113
	v_lshlrev_b32_e32 v138, 16, v110
	v_and_b32_e32 v139, 0xffff0000, v110
	v_lshlrev_b32_e32 v110, 16, v111
	v_and_b32_e32 v111, 0xffff0000, v111
	s_waitcnt vmcnt(13)
	v_lshlrev_b32_e32 v142, 16, v114
	v_and_b32_e32 v143, 0xffff0000, v114
	v_lshlrev_b32_e32 v114, 16, v115
	v_and_b32_e32 v115, 0xffff0000, v115
	s_waitcnt vmcnt(12)
	v_lshlrev_b32_e32 v144, 16, v116
	v_and_b32_e32 v145, 0xffff0000, v116
	v_lshlrev_b32_e32 v116, 16, v117
	v_and_b32_e32 v117, 0xffff0000, v117
	s_waitcnt vmcnt(10)
	v_lshlrev_b32_e32 v148, 16, v120
	v_and_b32_e32 v149, 0xffff0000, v120
	v_lshlrev_b32_e32 v120, 16, v121
	v_and_b32_e32 v121, 0xffff0000, v121
	s_waitcnt vmcnt(4)
	v_lshlrev_b32_e32 v160, 16, v132
	v_and_b32_e32 v161, 0xffff0000, v132
	v_lshlrev_b32_e32 v132, 16, v133
	v_and_b32_e32 v133, 0xffff0000, v133
	s_waitcnt vmcnt(2)
; DI unsigned pk2(float lo, float hi) { const f32x2 v = {lo, hi}; return __builtin_bit_cast(unsigned, __builtin_convertvector(v, bf16x2_t)); }
; template <int MODE, bool SB  > DI void norm_phase(const Params& P, const Frame& F, int L, const void* src_, const float* gain, bool combine) {
;     ...
; #pragma unroll
;             for (int j = 0; j < 8; ++j) { const f32x4 y1 = (f32x4){bflo(ya[j].x), bfhi(ya[j].x), bflo(ya[j].y), bfhi(ya[j].y)}, y2 = (f32x4){bflo(yb[j].x), bfhi(yb[j].x), bflo(yb[j].y), bfhi(yb[j].y)};
;                 v[j] = v[j] + w1 * y1 + w2 * y2;
;                 const u32x2 hb = {pk2(v[j][0], v[j][1]), pk2(v[j][2], v[j][3])}; *(u32x2*)(const_cast<bf16*>(srcb) + (size_t)row * D + 4 * F.lane + 256 * j) = hb;
;                 v[j] = (f32x4){bflo(hb.x), bfhi(hb.x), bflo(hb.y), bfhi(hb.y)}; }
;         }
;         float ss = 0.f;
; #pragma unroll
;         for (int j = 0; j < 8; ++j) ss += (v[j][0] * v[j][0] + v[j][1] * v[j][1]) + (v[j][2] * v[j][2] + v[j][3] * v[j][3]);
	v_lshlrev_b32_e32 v164, 16, v100
	v_and_b32_e32 v165, 0xffff0000, v100
	v_pk_fma_f32 v[44:45], v[102:103], v[136:137], v[44:45] op_sel_hi:[0,1,1]
	v_pk_fma_f32 v[46:47], v[102:103], v[108:109], v[46:47] op_sel_hi:[0,1,1]
	v_pk_fma_f32 v[48:49], v[102:103], v[140:141], v[48:49] op_sel_hi:[0,1,1]
	v_pk_fma_f32 v[50:51], v[102:103], v[112:113], v[50:51] op_sel_hi:[0,1,1]
	v_lshlrev_b32_e32 v146, 16, v118
	v_and_b32_e32 v147, 0xffff0000, v118
	v_lshlrev_b32_e32 v118, 16, v119
	v_and_b32_e32 v119, 0xffff0000, v119
	v_lshlrev_b32_e32 v150, 16, v122
	v_and_b32_e32 v151, 0xffff0000, v122
	v_lshlrev_b32_e32 v122, 16, v123
	v_and_b32_e32 v123, 0xffff0000, v123
	v_lshlrev_b32_e32 v152, 16, v124
	v_and_b32_e32 v153, 0xffff0000, v124
	v_lshlrev_b32_e32 v156, 16, v128
	v_and_b32_e32 v157, 0xffff0000, v128
	v_lshlrev_b32_e32 v162, 16, v134
	v_and_b32_e32 v163, 0xffff0000, v134
	v_lshlrev_b32_e32 v134, 16, v135
	v_and_b32_e32 v135, 0xffff0000, v135
	s_waitcnt vmcnt(1)
	v_lshlrev_b32_e32 v166, 16, v106
	v_and_b32_e32 v167, 0xffff0000, v106
	v_pk_fma_f32 v[52:53], v[102:103], v[144:145], v[52:53] op_sel_hi:[0,1,1]
	v_pk_fma_f32 v[54:55], v[102:103], v[116:117], v[54:55] op_sel_hi:[0,1,1]
	v_pk_fma_f32 v[56:57], v[102:103], v[148:149], v[56:57] op_sel_hi:[0,1,1]
	v_pk_fma_f32 v[58:59], v[102:103], v[120:121], v[58:59] op_sel_hi:[0,1,1]
	v_pk_fma_f32 v[68:69], v[102:103], v[160:161], v[68:69] op_sel_hi:[0,1,1]
	v_pk_fma_f32 v[70:71], v[102:103], v[132:133], v[70:71] op_sel_hi:[0,1,1]
	v_pk_fma_f32 v[72:73], v[102:103], v[164:165], v[72:73] op_sel_hi:[0,1,1]
	v_pk_fma_f32 v[46:47], v[104:105], v[110:111], v[46:47] op_sel_hi:[0,1,1]
	v_pk_fma_f32 v[44:45], v[104:105], v[138:139], v[44:45] op_sel_hi:[0,1,1]
	v_pk_fma_f32 v[50:51], v[104:105], v[114:115], v[50:51] op_sel_hi:[0,1,1]
	v_pk_fma_f32 v[48:49], v[104:105], v[142:143], v[48:49] op_sel_hi:[0,1,1]
	v_lshlrev_b32_e32 v154, 16, v126
	v_and_b32_e32 v155, 0xffff0000, v126
	v_lshlrev_b32_e32 v158, 16, v130
	v_and_b32_e32 v159, 0xffff0000, v130
	v_pk_fma_f32 v[60:61], v[102:103], v[152:153], v[60:61] op_sel_hi:[0,1,1]
	v_pk_fma_f32 v[64:65], v[102:103], v[156:157], v[64:65] op_sel_hi:[0,1,1]
	v_pk_fma_f32 v[54:55], v[104:105], v[118:119], v[54:55] op_sel_hi:[0,1,1]
	v_pk_fma_f32 v[52:53], v[104:105], v[146:147], v[52:53] op_sel_hi:[0,1,1]
	v_pk_fma_f32 v[58:59], v[104:105], v[122:123], v[58:59] op_sel_hi:[0,1,1]
	v_pk_fma_f32 v[56:57], v[104:105], v[150:151], v[56:57] op_sel_hi:[0,1,1]
	v_pk_fma_f32 v[70:71], v[104:105], v[134:135], v[70:71] op_sel_hi:[0,1,1]
	v_pk_fma_f32 v[68:69], v[104:105], v[162:163], v[68:69] op_sel_hi:[0,1,1]
	v_pk_fma_f32 v[72:73], v[104:105], v[166:167], v[72:73] op_sel_hi:[0,1,1]
	v_cvt_pk_bf16_f32 v44, v44, v45
	v_cvt_pk_bf16_f32 v45, v46, v47
	v_cvt_pk_bf16_f32 v46, v48, v49
	v_cvt_pk_bf16_f32 v47, v50, v51
	v_lshlrev_b32_e32 v124, 16, v125
	v_and_b32_e32 v125, 0xffff0000, v125
	v_lshlrev_b32_e32 v128, 16, v129
	v_and_b32_e32 v129, 0xffff0000, v129
	v_lshlrev_b32_e32 v100, 16, v101
	v_and_b32_e32 v101, 0xffff0000, v101
	v_pk_fma_f32 v[60:61], v[104:105], v[154:155], v[60:61] op_sel_hi:[0,1,1]
	v_pk_fma_f32 v[64:65], v[104:105], v[158:159], v[64:65] op_sel_hi:[0,1,1]
	v_cvt_pk_bf16_f32 v48, v52, v53
	v_cvt_pk_bf16_f32 v49, v54, v55
	v_cvt_pk_bf16_f32 v50, v56, v57
	v_cvt_pk_bf16_f32 v51, v58, v59
	v_cvt_pk_bf16_f32 v56, v68, v69
	v_cvt_pk_bf16_f32 v57, v70, v71
	v_cvt_pk_bf16_f32 v58, v72, v73
	global_store_dwordx2 v[98:99], v[44:45], off
	global_store_dwordx2 v[98:99], v[46:47], off offset:512
	global_store_dwordx2 v[98:99], v[48:49], off offset:1024
	global_store_dwordx2 v[98:99], v[50:51], off offset:1536
	v_lshlrev_b32_e32 v68, 16, v44
	v_and_b32_e32 v69, 0xffff0000, v44
	v_lshlrev_b32_e32 v44, 16, v45
	v_and_b32_e32 v45, 0xffff0000, v45
	v_lshlrev_b32_e32 v71, 16, v47
	v_lshlrev_b32_e32 v70, 16, v46
	v_and_b32_e32 v47, 0xffff0000, v47
	v_and_b32_e32 v46, 0xffff0000, v46
	v_lshlrev_b32_e32 v126, 16, v127
	v_and_b32_e32 v127, 0xffff0000, v127
	v_lshlrev_b32_e32 v130, 16, v131
	v_and_b32_e32 v131, 0xffff0000, v131
	v_lshlrev_b32_e32 v106, 16, v107
	v_and_b32_e32 v107, 0xffff0000, v107
	v_pk_fma_f32 v[62:63], v[102:103], v[124:125], v[62:63] op_sel_hi:[0,1,1]
	v_pk_fma_f32 v[66:67], v[102:103], v[128:129], v[66:67] op_sel_hi:[0,1,1]
	v_pk_fma_f32 v[74:75], v[102:103], v[100:101], v[74:75] op_sel_hi:[0,1,1]
	v_cvt_pk_bf16_f32 v52, v60, v61
	v_cvt_pk_bf16_f32 v54, v64, v65
	v_lshlrev_b32_e32 v61, 16, v50
	v_lshlrev_b32_e32 v65, 16, v58
	v_and_b32_e32 v73, 0xffff0000, v48
	v_mul_f32_e32 v60, v45, v45
	v_pk_mul_f32 v[102:103], v[46:47], v[46:47]
	v_mul_f32_e32 v64, v69, v69
	v_pk_fma_f32 v[62:63], v[104:105], v[126:127], v[62:63] op_sel_hi:[0,1,1]
	v_pk_fma_f32 v[66:67], v[104:105], v[130:131], v[66:67] op_sel_hi:[0,1,1]
	v_pk_fma_f32 v[74:75], v[104:105], v[106:107], v[74:75] op_sel_hi:[0,1,1]
	v_lshlrev_b32_e32 v72, 16, v48
	v_lshlrev_b32_e32 v48, 16, v49
	v_and_b32_e32 v49, 0xffff0000, v49
	v_mov_b32_e32 v105, v61
	v_mul_f32_e32 v104, v73, v73
	v_mov_b32_e32 v116, v70
	v_mov_b32_e32 v117, v46
	v_mov_b32_e32 v46, v71
	v_pk_fma_f32 v[122:123], v[44:45], v[44:45], v[60:61] op_sel_hi:[1,1,0]
	v_pk_fma_f32 v[70:71], v[70:71], v[70:71], v[102:103]
	v_pk_fma_f32 v[102:103], v[68:69], v[68:69], v[64:65] op_sel_hi:[1,1,0]
	v_cvt_pk_bf16_f32 v53, v62, v63
	v_and_b32_e32 v63, 0xffff0000, v50
	v_lshlrev_b32_e32 v50, 16, v51
	v_and_b32_e32 v51, 0xffff0000, v51
	v_mul_f32_e32 v106, v49, v49
	v_mov_b32_e32 v107, v65
	v_pk_fma_f32 v[124:125], v[72:73], v[72:73], v[104:105] op_sel_hi:[1,1,0]
	v_mov_b32_e32 v60, v102
	v_mov_b32_e32 v104, v122
	v_mul_f32_e32 v113, v63, v63
	v_mul_f32_e32 v115, v50, v50
; DI unsigned pk2(float lo, float hi) { const f32x2 v = {lo, hi}; return __builtin_bit_cast(unsigned, __builtin_convertvector(v, bf16x2_t)); }
; DI float wave_sum(float v) { v += shx<1>(v); v += shx<2>(v); v += shx<4>(v); v += shx<8>(v); v += shx<16>(v); v += shx<32>(v); return v; }
; template <int MODE, bool SB  > DI void norm_phase(const Params& P, const Frame& F, int L, const void* src_, const float* gain, bool combine) {
;     ...
;                 const u32x2 hb = {pk2(v[j][0], v[j][1]), pk2(v[j][2], v[j][3])}; *(u32x2*)(const_cast<bf16*>(srcb) + (size_t)row * D + 4 * F.lane + 256 * j) = hb;
;                 v[j] = (f32x4){bflo(hb.x), bfhi(hb.x), bflo(hb.y), bfhi(hb.y)}; }
;         }
;         float ss = 0.f;
; #pragma unroll
;         for (int j = 0; j < 8; ++j) ss += (v[j][0] * v[j][0] + v[j][1] * v[j][1]) + (v[j][2] * v[j][2] + v[j][3] * v[j][3]);
;         const float rstd = 1.0f / sqrtf(wave_sum(ss) * (1.0f / D) + EPS);
	v_mul_f32_e32 v128, v51, v51
	v_mov_b32_e32 v62, v61
	v_pk_fma_f32 v[126:127], v[48:49], v[48:49], v[106:107] op_sel_hi:[1,1,0]
	v_pk_add_f32 v[102:103], v[102:103], v[122:123]
	v_pk_add_f32 v[70:71], v[70:71], v[70:71] op_sel:[0,1] op_sel_hi:[1,0]
	v_pk_mul_f32 v[60:61], v[60:61], v[104:105]
	v_cvt_pk_bf16_f32 v55, v66, v67
	v_cvt_pk_bf16_f32 v59, v74, v75
	global_store_dwordx2 v[98:99], v[52:53], off offset:2048
	global_store_dwordx2 v[98:99], v[54:55], off offset:2560
	global_store_dwordx2 v[98:99], v[56:57], off offset:3072
	global_store_dwordx2 v[98:99], v[58:59], off offset:3584
	v_lshlrev_b32_e32 v75, 16, v53
	v_lshlrev_b32_e32 v74, 16, v52
	v_and_b32_e32 v53, 0xffff0000, v53
	v_and_b32_e32 v52, 0xffff0000, v52
	v_mov_b32_e32 v125, v115
	v_mov_b32_e32 v127, v128
	v_mov_b32_e32 v71, v113
	v_mov_b32_e32 v103, v61
	v_pk_mul_f32 v[108:109], v[52:53], v[52:53]
	v_pk_add_f32 v[104:105], v[124:125], v[126:127]
	v_pk_add_f32 v[60:61], v[102:103], v[70:71]
	v_lshlrev_b32_e32 v99, 16, v55
	v_lshlrev_b32_e32 v98, 16, v54
	v_and_b32_e32 v55, 0xffff0000, v55
	v_and_b32_e32 v54, 0xffff0000, v54
	v_mov_b32_e32 v118, v74
	v_mov_b32_e32 v119, v52
	v_mov_b32_e32 v52, v75
	v_pk_fma_f32 v[74:75], v[74:75], v[74:75], v[108:109]
	v_pk_add_f32 v[60:61], v[60:61], v[104:105]
	v_lshlrev_b32_e32 v100, 16, v56
	v_and_b32_e32 v101, 0xffff0000, v56
	v_lshlrev_b32_e32 v56, 16, v57
	v_and_b32_e32 v57, 0xffff0000, v57
	v_pk_mul_f32 v[110:111], v[54:55], v[54:55]
	v_pk_add_f32 v[74:75], v[74:75], v[74:75] op_sel:[0,1] op_sel_hi:[1,0]
	v_pk_add_f32 v[60:61], v[60:61], v[60:61] op_sel:[0,1] op_sel_hi:[1,0]
	v_and_b32_e32 v67, 0xffff0000, v58
	v_lshlrev_b32_e32 v58, 16, v59
	v_and_b32_e32 v59, 0xffff0000, v59
	v_mul_f32_e32 v112, v101, v101
	v_mul_f32_e32 v114, v57, v57
	v_mov_b32_e32 v120, v98
	v_mov_b32_e32 v121, v54
	v_mov_b32_e32 v54, v99
	v_pk_fma_f32 v[98:99], v[98:99], v[98:99], v[110:111]
	v_mov_b32_e32 v106, v74
	v_mov_b32_e32 v64, v60
	v_mul_f32_e32 v129, v67, v67
	v_mul_f32_e32 v130, v58, v58
	v_mul_f32_e32 v131, v59, v59
	v_mov_b32_e32 v66, v65
	v_pk_fma_f32 v[108:109], v[100:101], v[100:101], v[112:113] op_sel_hi:[1,1,0]
	v_pk_fma_f32 v[110:111], v[56:57], v[56:57], v[114:115] op_sel_hi:[1,1,0]
	v_pk_add_f32 v[98:99], v[98:99], v[98:99] op_sel:[0,1] op_sel_hi:[1,0]
	v_pk_add_f32 v[60:61], v[60:61], v[74:75]
	v_pk_mul_f32 v[64:65], v[64:65], v[106:107]
	v_mov_b32_e32 v109, v130
	v_mov_b32_e32 v111, v131
	v_mov_b32_e32 v99, v129
	v_mov_b32_e32 v61, v65
	v_pk_add_f32 v[108:109], v[108:109], v[110:111]
	v_pk_add_f32 v[60:61], v[60:61], v[98:99]
	s_nop 0
	v_pk_add_f32 v[60:61], v[60:61], v[108:109]
	s_nop 0
	v_add_f32_e32 v60, v60, v61
	s_nop 1
	v_add_f32_dpp v60, v60, v60 quad_perm:[1,0,3,2] row_mask:0xf bank_mask:0xf bound_ctrl:1
	s_nop 1
	v_add_f32_dpp v60, v60, v60 quad_perm:[2,3,0,1] row_mask:0xf bank_mask:0xf bound_ctrl:1
	ds_swizzle_b32 v61, v60 offset:swizzle(SWAP,4)
	s_waitcnt lgkmcnt(0)
	v_add_f32_e32 v60, v60, v61
	ds_swizzle_b32 v61, v60 offset:swizzle(SWAP,8)
	s_waitcnt lgkmcnt(0)
	v_add_f32_e32 v60, v60, v61
	ds_swizzle_b32 v61, v60 offset:swizzle(SWAP,16)
	s_waitcnt lgkmcnt(0)
	v_add_f32_e32 v60, v60, v61
	ds_bpermute_b32 v61, v94, v60
	s_waitcnt lgkmcnt(0)
; DI unsigned pk2(float lo, float hi) { const f32x2 v = {lo, hi}; return __builtin_bit_cast(unsigned, __builtin_convertvector(v, bf16x2_t)); }
; DI unsigned pk4_fp8(float a, float b, float c, float d) { unsigned w = 0u; w = __builtin_amdgcn_cvt_pk_fp8_f32(a, b, w, false); w = __builtin_amdgcn_cvt_pk_fp8_f32(c, d, w, true); return w; }
; DI float wave_sum(float v) { v += shx<1>(v); v += shx<2>(v); v += shx<4>(v); v += shx<8>(v); v += shx<16>(v); v += shx<32>(v); return v; }
; template <int MODE, bool SB  > DI void norm_phase(const Params& P, const Frame& F, int L, const void* src_, const float* gain, bool combine) {
;     ...
;         const float rstd = 1.0f / sqrtf(wave_sum(ss) * (1.0f / D) + EPS);
; #pragma unroll
;         for (int j = 0; j < 8; ++j) v[j] = v[j] * rstd * g[j];
;         if (MODE == 4) {
; #pragma unroll
;             for (int j = 0; j < 8; ++j) *(f32x4*)(P.out + (size_t)row * D + 4 * F.lane + 256 * j) = v[j];
;         } else if (MODE == 0 || MODE == 2 || (MODE == 3 && L == 1)) {
;             unsigned* o4 = (unsigned*)((unsigned char*)HN + (size_t)row * D) + F.lane; const float hs = (float)(1 << LS_HN);
; #pragma unroll
;             for (int j = 0; j < 8; ++j) o4[64 * j] = pk4_fp8(v[j][0] * hs, v[j][1] * hs, v[j][2] * hs, v[j][3] * hs);
;     ...
;         if (MODE == 3) { const f32x4 pv = *(const f32x4*)(P.in[I_P] + ((size_t)L * M + row) * PLE + 4 * F.lane);
;             *((unsigned long long*)((bf16*)(ws + WS_T + T_PB) + (size_t)row * PLE) + F.lane) = (unsigned long long)pk2(pv[0], pv[1]) | ((unsigned long long)pk2(pv[2], pv[3]) << 32); }
	v_add_f32_e32 v60, v60, v61
	v_fmamk_f32 v60, v60, 0x3a000000, v96
	v_mul_f32_e32 v61, 0x4f800000, v60
	v_cmp_gt_f32_e32 vcc, s21, v60
	s_nop 1
	v_cndmask_b32_e32 v60, v60, v61, vcc
	v_sqrt_f32_e32 v61, v60
	s_nop 0
	v_add_u32_e32 v64, -1, v61
	v_add_u32_e32 v65, 1, v61
	v_fma_f32 v70, -v64, v61, v60
	v_fma_f32 v71, -v65, v61, v60
	v_cmp_ge_f32_e64 s[4:5], 0, v70
	s_nop 1
	v_cndmask_b32_e64 v61, v61, v64, s[4:5]
	v_cmp_lt_f32_e64 s[4:5], 0, v71
	s_nop 1
	v_cndmask_b32_e64 v61, v61, v65, s[4:5]
	v_mul_f32_e32 v64, 0x37800000, v61
	v_cndmask_b32_e32 v61, v61, v64, vcc
	v_cmp_class_f32_e32 vcc, v60, v97
	s_nop 1
	v_cndmask_b32_e32 v60, v61, v60, vcc
	v_div_scale_f32 v61, s[4:5], v60, v60, 1.0
	v_rcp_f32_e32 v65, v61
	v_div_scale_f32 v64, vcc, 1.0, v60, 1.0
	s_mov_b32 s4, s23
	v_fma_f32 v70, -v61, v65, 1.0
	v_fmac_f32_e32 v65, v70, v65
	v_mul_f32_e32 v70, v64, v65
	v_fma_f32 v71, -v61, v70, v64
	v_fmac_f32_e32 v70, v71, v65
	v_fma_f32 v61, -v61, v70, v64
	v_div_fmas_f32 v61, v61, v65, v70
	v_div_fixup_f32 v60, v61, v60, 1.0
	v_pk_mul_f32 v[64:65], v[60:61], v[68:69] op_sel_hi:[0,1]
	v_pk_mul_f32 v[44:45], v[60:61], v[44:45] op_sel_hi:[0,1]
	v_pk_mul_f32 v[68:69], v[60:61], v[116:117] op_sel_hi:[0,1]
	v_pk_mul_f32 v[46:47], v[60:61], v[46:47] op_sel_hi:[0,1]
	v_pk_mul_f32 v[70:71], v[60:61], v[72:73] op_sel_hi:[0,1]
	v_pk_mul_f32 v[48:49], v[60:61], v[48:49] op_sel_hi:[0,1]
	v_pk_mul_f32 v[62:63], v[62:63], v[60:61] op_sel_hi:[1,0]
	v_pk_mul_f32 v[50:51], v[50:51], v[60:61] op_sel_hi:[1,0]
	v_pk_mul_f32 v[72:73], v[60:61], v[118:119] op_sel_hi:[0,1]
	v_pk_mul_f32 v[52:53], v[60:61], v[52:53] op_sel_hi:[0,1]
	v_pk_mul_f32 v[74:75], v[60:61], v[120:121] op_sel_hi:[0,1]
	v_pk_mul_f32 v[54:55], v[60:61], v[54:55] op_sel_hi:[0,1]
	v_pk_mul_f32 v[98:99], v[60:61], v[100:101] op_sel_hi:[0,1]
	v_pk_mul_f32 v[56:57], v[60:61], v[56:57] op_sel_hi:[0,1]
	v_pk_mul_f32 v[66:67], v[66:67], v[60:61] op_sel_hi:[1,0]
	v_pk_mul_f32 v[58:59], v[58:59], v[60:61] op_sel_hi:[1,0]
	v_pk_mul_f32 v[60:61], v[8:9], v[64:65]
	v_pk_mul_f32 v[64:65], v[0:1], v[68:69]
	v_mul_f32_e32 v60, 4.0, v60
	v_mul_f32_e32 v61, 4.0, v61
	v_pk_mul_f32 v[68:69], v[4:5], v[70:71]
	v_mul_f32_e32 v64, 4.0, v64
	v_mul_f32_e32 v65, 4.0, v65
	v_cvt_pk_fp8_f32 v168, v60, v61
	v_pk_mul_f32 v[62:63], v[12:13], v[62:63]
	v_mul_f32_e32 v68, 4.0, v68
	v_mul_f32_e32 v69, 4.0, v69
	v_cvt_pk_fp8_f32 v169, v64, v65
	v_pk_mul_f32 v[44:45], v[10:11], v[44:45]
	v_pk_mul_f32 v[70:71], v[16:17], v[72:73]
	v_pk_mul_f32 v[72:73], v[20:21], v[74:75]
	v_pk_mul_f32 v[74:75], v[24:25], v[98:99]
	v_pk_mul_f32 v[66:67], v[28:29], v[66:67]
	v_mul_f32_e32 v62, 4.0, v62
	v_mul_f32_e32 v63, 4.0, v63
	v_cvt_pk_fp8_f32 v170, v68, v69
	v_pk_mul_f32 v[46:47], v[2:3], v[46:47]
	v_mul_f32_e32 v44, 4.0, v44
	v_mul_f32_e32 v45, 4.0, v45
	v_mul_f32_e32 v70, 4.0, v70
	v_mul_f32_e32 v71, 4.0, v71
	v_mul_f32_e32 v72, 4.0, v72
	v_mul_f32_e32 v73, 4.0, v73
	v_mul_f32_e32 v74, 4.0, v74
	v_mul_f32_e32 v75, 4.0, v75
	v_mul_f32_e32 v66, 4.0, v66
	v_mul_f32_e32 v67, 4.0, v67
	v_cvt_pk_fp8_f32 v171, v62, v63
	v_pk_mul_f32 v[48:49], v[6:7], v[48:49]
	v_mul_f32_e32 v46, 4.0, v46
	v_mul_f32_e32 v47, 4.0, v47
	v_cvt_pk_fp8_f32 v172, v70, v71
	v_cvt_pk_fp8_f32 v173, v72, v73
	v_cvt_pk_fp8_f32 v174, v74, v75
	v_cvt_pk_fp8_f32 v175, v66, v67
	v_cvt_pk_fp8_f32 v168, v44, v45 op_sel:[0,0,1]
	v_pk_mul_f32 v[50:51], v[14:15], v[50:51]
	v_mul_f32_e32 v48, 4.0, v48
	v_mul_f32_e32 v49, 4.0, v49
	v_cvt_pk_fp8_f32 v169, v46, v47 op_sel:[0,0,1]
	v_pk_mul_f32 v[52:53], v[18:19], v[52:53]
	v_pk_mul_f32 v[54:55], v[22:23], v[54:55]
	v_pk_mul_f32 v[56:57], v[26:27], v[56:57]
	v_pk_mul_f32 v[58:59], v[30:31], v[58:59]
	v_mul_f32_e32 v50, 4.0, v50
	v_mul_f32_e32 v51, 4.0, v51
	v_cvt_pk_fp8_f32 v170, v48, v49 op_sel:[0,0,1]
	v_mul_f32_e32 v52, 4.0, v52
	v_mul_f32_e32 v53, 4.0, v53
	v_mul_f32_e32 v54, 4.0, v54
	v_mul_f32_e32 v55, 4.0, v55
	v_mul_f32_e32 v56, 4.0, v56
	v_mul_f32_e32 v57, 4.0, v57
	v_mul_f32_e32 v58, 4.0, v58
	v_mul_f32_e32 v59, 4.0, v59
	v_cvt_pk_fp8_f32 v171, v50, v51 op_sel:[0,0,1]
	v_cvt_pk_fp8_f32 v172, v52, v53 op_sel:[0,0,1]
	v_cvt_pk_fp8_f32 v173, v54, v55 op_sel:[0,0,1]
	v_cvt_pk_fp8_f32 v174, v56, v57 op_sel:[0,0,1]
	v_cvt_pk_fp8_f32 v175, v58, v59 op_sel:[0,0,1]
	global_store_dword v[92:93], v168, off
	global_store_dword v[92:93], v169, off offset:256
	global_store_dword v[92:93], v170, off offset:512
	global_store_dword v[92:93], v171, off offset:768
	global_store_dword v[92:93], v172, off offset:1024
	global_store_dword v[92:93], v173, off offset:1280
	global_store_dword v[92:93], v174, off offset:1536
	global_store_dword v[92:93], v175, off offset:1792
	v_lshl_add_u64 v[48:49], s[54:55], 0, v[36:37]
	v_lshl_add_u64 v[36:37], v[36:37], 0, s[8:9]
	s_and_b64 vcc, s[14:15], exec
	v_lshl_add_u64 v[38:39], v[38:39], 0, s[0:1]
	s_waitcnt vmcnt(16)
	v_cvt_pk_bf16_f32 v44, v176, v177
	v_cvt_pk_bf16_f32 v45, v178, v179
	global_store_dwordx2 v[48:49], v[44:45], off
	s_cbranch_vccnz .LBB0_3245

.LBB0_3291:
	s_cmp_lt_u32 s3, 0x40001
	s_mov_b64 s[18:19], 0
	s_cselect_b64 s[20:21], -1, 0
	s_mov_b64 s[22:23], -1
	s_and_b64 vcc, exec, s[20:21]
	s_cbranch_vccnz .LBB0_3288
	s_branch .LBB0_3285
	s_nop 0
	s_nop 0
.LBB0_3292:
	s_or_b64 exec, exec, s[14:15]
	s_and_b64 s[14:15], s[16:17], exec

; __device__ __forceinline__ unsigned xb_add(unsigned* p, unsigned v) { return __hip_atomic_fetch_add(p, v, __ATOMIC_RELAXED, __HIP_MEMORY_SCOPE_AGENT); }
; __device__ __forceinline__ void xcd_barrier(const XcdBarrier& b) {
;     ...
;             __builtin_amdgcn_fence(__ATOMIC_ACQUIRE, "agent");
;             xb_add(&bar[XB_XGEN(b.x)], 1u);
;             asm volatile("s_waitcnt vmcnt(0)" ::: "memory");
.LBB0_3296:
	s_or_b64 exec, exec, s[6:7]
	s_mov_b64 s[6:7], exec
	v_mbcnt_lo_u32_b32 v0, s6, 0
	v_mbcnt_hi_u32_b32 v0, s7, v0
	v_cmp_eq_u32_e32 vcc, 0, v0
	s_waitcnt vmcnt(0)
	buffer_inv sc1
	s_and_saveexec_b64 s[8:9], vcc
	s_cbranch_execz .LBB0_3298
	s_bcnt1_i32_b64 s3, s[6:7]
	v_mov_b32_e32 v0, 0x2000
	v_mov_b32_e32 v1, s3
.LBB0_3298:
	s_or_b64 exec, exec, s[8:9]
	s_waitcnt vmcnt(0)

; __device__ __forceinline__ unsigned xb_add(unsigned* p, unsigned v) { return __hip_atomic_fetch_add(p, v, __ATOMIC_RELAXED, __HIP_MEMORY_SCOPE_AGENT); }
; __device__ __forceinline__ void xcd_barrier(const XcdBarrier& b) {
;     ...
;             __builtin_amdgcn_fence(__ATOMIC_ACQUIRE, "agent");
;             xb_add(&bar[XB_XGEN(b.x)], 1u);
;             asm volatile("s_waitcnt vmcnt(0)" ::: "memory");
.LBB0_3400:
	s_or_b64 exec, exec, s[6:7]
	s_mov_b64 s[6:7], exec
	v_mbcnt_lo_u32_b32 v0, s6, 0
	v_mbcnt_hi_u32_b32 v0, s7, v0
	v_cmp_eq_u32_e32 vcc, 0, v0
	s_waitcnt vmcnt(0)
	buffer_inv sc1
	s_and_saveexec_b64 s[8:9], vcc
	s_cbranch_execz .LBB0_3402
	s_bcnt1_i32_b64 s3, s[6:7]
	v_mov_b32_e32 v0, 0x2000
	v_mov_b32_e32 v1, s3
.LBB0_3402:
	s_or_b64 exec, exec, s[8:9]
	s_waitcnt vmcnt(0)

; __device__ __forceinline__ unsigned xb_add(unsigned* p, unsigned v) { return __hip_atomic_fetch_add(p, v, __ATOMIC_RELAXED, __HIP_MEMORY_SCOPE_AGENT); }
; __device__ __forceinline__ void xcd_barrier(const XcdBarrier& b) {
;     ...
;             __builtin_amdgcn_fence(__ATOMIC_ACQUIRE, "agent");
;             xb_add(&bar[XB_XGEN(b.x)], 1u);
;             asm volatile("s_waitcnt vmcnt(0)" ::: "memory");
.LBB0_3458:
	s_or_b64 exec, exec, s[4:5]
	s_mov_b64 s[4:5], exec
	v_mbcnt_lo_u32_b32 v0, s4, 0
	v_mbcnt_hi_u32_b32 v0, s5, v0
	v_cmp_eq_u32_e32 vcc, 0, v0
	s_waitcnt vmcnt(0)
	buffer_inv sc1
	s_and_saveexec_b64 s[6:7], vcc
	s_cbranch_execz .LBB0_3460
	s_bcnt1_i32_b64 s4, s[4:5]
	v_mov_b32_e32 v0, 0x2000
	v_mov_b32_e32 v1, s4
.LBB0_3460:
	s_or_b64 exec, exec, s[6:7]
	s_waitcnt vmcnt(0)
